# lru_combine loop software-pipelined (next iteration loads prefetched, vmcnt(6) leaves store outstanding, fused bf16 packs)
# speedup vs baseline: 1.0034x; 1.0034x over previous
; __device__ __forceinline__ unsigned pk2(float lo, float hi) { return f2bf(lo) | (f2bf(hi) << 16); }
; __device__ __forceinline__ float gelu_tanh(float x) { const float y = 0.7978845608028654f * (x + 0.044715f * x * x * x); const float e = __expf(2.0f * y); return x * (1.0f - __builtin_amdgcn_rcpf(1.0f + e)); }
; __device__ __forceinline__ void lru_combine(const Params& P, size_t wi, size_t nw) {
;     unsigned char* ws = P.ws;
;     const v4u* HLOC = (const v4u*)(ws + WS_HLOC); const v4u* PCUM = (const v4u*)(ws + WS_PCUM); const v4u* GATE = (const v4u*)(ws + WS_GATE);
;     const float* HIN = (const float*)(ws + WS_HIN); bf16* Y = (bf16*)((unsigned char*)P.out + OUT_Y);
;     for (size_t i = wi; i < (size_t)T * 64; i += nw) {
;         const size_t t = i >> 6; const int ch0 = (int)(i & 63) * 8;
;         const v4u hl = HLOC[i], pc = PCUM[i], gt = GATE[i];
;         const f32x4 h0 = *(const f32x4*)(HIN + (t >> 6) * 512 + ch0), h1 = *(const f32x4*)(HIN + (t >> 6) * 512 + ch0 + 4);
;         float y[8];
;         y[0] = (bflo(hl.x) + bflo(pc.x) * h0.x) * gelu_tanh(bflo(gt.x)); y[1] = (bfhi(hl.x) + bfhi(pc.x) * h0.y) * gelu_tanh(bfhi(gt.x));
;         y[2] = (bflo(hl.y) + bflo(pc.y) * h0.z) * gelu_tanh(bflo(gt.y)); y[3] = (bfhi(hl.y) + bfhi(pc.y) * h0.w) * gelu_tanh(bfhi(gt.y));
;         y[4] = (bflo(hl.z) + bflo(pc.z) * h1.x) * gelu_tanh(bflo(gt.z)); y[5] = (bfhi(hl.z) + bfhi(pc.z) * h1.y) * gelu_tanh(bfhi(gt.z));
;         y[6] = (bflo(hl.w) + bflo(pc.w) * h1.z) * gelu_tanh(bflo(gt.w)); y[7] = (bfhi(hl.w) + bfhi(pc.w) * h1.w) * gelu_tanh(bfhi(gt.w));
;         v4u o; o.x = pk2(y[0], y[1]); o.y = pk2(y[2], y[3]); o.z = pk2(y[4], y[5]); o.w = pk2(y[6], y[7]);
;         *(v4u*)(Y + t * 1024 + 512 + ch0) = o;
.LBB0_2046:
	s_or_b64 exec, exec, s[0:1]
	s_lshl_b64 s[0:1], s[14:15], 9
	v_or_b32_e32 v2, s0, v0
	v_mov_b32_e32 v3, s1
	s_mov_b64 s[0:1], 0x100000
	v_cmp_gt_u64_e32 vcc, s[0:1], v[2:3]
	s_barrier
	s_and_saveexec_b64 s[6:7], vcc
	s_cbranch_execz .LBB0_2049
	s_ashr_i32 s13, s12, 31
	s_lshl_b64 s[16:17], s[12:13], 9
	s_add_u32 s18, s24, 0x280000
	s_addc_u32 s19, s25, 0
	s_lshl_b64 s[0:1], s[14:15], 13
	v_lshl_or_b32 v6, v0, 4, s0
	v_mov_b32_e32 v7, s1
	s_lshl_b64 s[0:1], s[14:15], 12
	v_mov_b32_e32 v5, 0
	s_lshl_b64 s[20:21], s[12:13], 13
	v_lshl_or_b32 v8, v0, 3, s0
	v_mov_b32_e32 v9, s1
	s_lshl_b64 s[12:13], s[12:13], 12
	s_mov_b64 s[14:15], 0
	s_mov_b32 s3, 0xffff0000
	s_movk_i32 s22, 0x7fff
	s_mov_b64 s[42:43], 0xfffff
	v_mov_b32_e32 v87, 0
	v_lshl_add_u64 v[10:11], s[24:25], 0, v[6:7]
	v_add_co_u32_e32 v12, vcc, 0x1c00000, v10
	v_lshrrev_b32_e32 v4, 1, v2
	s_nop 0
	v_addc_co_u32_e32 v13, vcc, 0, v11, vcc
	v_add_co_u32_e32 v16, vcc, 0x2c00000, v10
	v_and_b32_e32 v1, 0x1f8, v8
	v_and_b32_e32 v4, 0x7f800, v4
	v_addc_co_u32_e32 v17, vcc, 0, v11, vcc
	v_lshl_add_u64 v[18:19], s[18:19], 0, v[4:5]
	v_lshlrev_b32_e32 v4, 2, v1
	v_add_co_u32_e32 v10, vcc, 0x8c00000, v10
	v_and_b32_e32 v20, 0xfffc00, v6
	v_lshl_add_u64 v[28:29], v[18:19], 0, v[4:5]
	v_addc_co_u32_e32 v11, vcc, 0, v11, vcc
	global_load_dwordx4 v[12:15], v[12:13], off
	v_lshlrev_b32_e32 v4, 1, v20
	global_load_dwordx4 v[16:19], v[16:17], off
	s_nop 0
	global_load_dwordx4 v[20:23], v[28:29], off offset:16
	global_load_dwordx4 v[24:27], v[10:11], off
	s_nop 0
	global_load_dwordx4 v[28:31], v[28:29], off
	v_lshl_add_u64 v[32:33], s[94:95], 0, v[4:5]
	v_lshlrev_b32_e32 v4, 1, v1
	v_lshl_add_u64 v[10:11], v[32:33], 0, v[4:5]
	v_add_co_u32_e32 v32, vcc, 0x400000, v10
	v_lshl_add_u64 v[2:3], v[2:3], 0, s[16:17]
	s_nop 0
	v_addc_co_u32_e32 v33, vcc, 0, v11, vcc
	v_cmp_lt_u64_e64 s[0:1], s[42:43], v[2:3]
	v_lshl_add_u64 v[6:7], v[6:7], 0, s[20:21]
	v_lshl_add_u64 v[8:9], v[8:9], 0, s[12:13]
	s_or_b64 s[14:15], s[0:1], s[14:15]
	s_mov_b64 s[98:99], exec
	s_andn2_b64 exec, exec, s[14:15]
	s_cbranch_execz .Llc_lastA
	v_lshl_add_u64 v[50:51], s[24:25], 0, v[6:7]
	v_add_co_u32_e32 v52, vcc, 0x1c00000, v50
	v_lshrrev_b32_e32 v86, 1, v2
	s_nop 0
	v_addc_co_u32_e32 v53, vcc, 0, v51, vcc
	v_add_co_u32_e32 v56, vcc, 0x2c00000, v50
	v_and_b32_e32 v88, 0x1f8, v8
	v_and_b32_e32 v86, 0x7f800, v86
	v_addc_co_u32_e32 v57, vcc, 0, v51, vcc
	v_lshl_add_u64 v[58:59], s[18:19], 0, v[86:87]
	v_lshlrev_b32_e32 v86, 2, v88
	v_add_co_u32_e32 v50, vcc, 0x8c00000, v50
	v_and_b32_e32 v60, 0xfffc00, v6
	v_lshl_add_u64 v[68:69], v[58:59], 0, v[86:87]
	v_addc_co_u32_e32 v51, vcc, 0, v51, vcc
	global_load_dwordx4 v[52:55], v[52:53], off
	v_lshlrev_b32_e32 v86, 1, v60
	global_load_dwordx4 v[56:59], v[56:57], off
	s_nop 0
	global_load_dwordx4 v[60:63], v[68:69], off offset:16
	global_load_dwordx4 v[64:67], v[50:51], off
	s_nop 0
	global_load_dwordx4 v[68:71], v[68:69], off
	v_lshl_add_u64 v[72:73], s[94:95], 0, v[86:87]
	v_lshlrev_b32_e32 v86, 1, v88
	v_lshl_add_u64 v[50:51], v[72:73], 0, v[86:87]
	v_add_co_u32_e32 v72, vcc, 0x400000, v50
	v_lshl_add_u64 v[2:3], v[2:3], 0, s[16:17]
	s_nop 0
	v_addc_co_u32_e32 v73, vcc, 0, v51, vcc
	v_cmp_lt_u64_e64 s[0:1], s[42:43], v[2:3]
	v_lshl_add_u64 v[6:7], v[6:7], 0, s[20:21]
	v_lshl_add_u64 v[8:9], v[8:9], 0, s[12:13]
	s_or_b64 s[14:15], s[0:1], s[14:15]
	s_mov_b64 s[100:101], exec
	s_mov_b64 exec, s[98:99]
	s_waitcnt vmcnt(5)
	v_lshlrev_b32_e32 v11, 16, v13
	v_lshlrev_b32_e32 v10, 16, v12
	v_and_b32_e32 v13, 0xffff0000, v13
	v_and_b32_e32 v12, 0xffff0000, v12
	v_lshlrev_b32_e32 v35, 16, v15
	v_lshlrev_b32_e32 v34, 16, v14
	v_and_b32_e32 v15, 0xffff0000, v15
	v_and_b32_e32 v14, 0xffff0000, v14
	v_lshlrev_b32_e32 v37, 16, v17
	v_lshlrev_b32_e32 v36, 16, v16
	v_and_b32_e32 v17, 0xffff0000, v17
	v_and_b32_e32 v16, 0xffff0000, v16
	v_lshlrev_b32_e32 v39, 16, v19
	v_lshlrev_b32_e32 v38, 16, v18
	v_mov_b32_e32 v40, v20
	v_mov_b32_e32 v41, v22
	v_and_b32_e32 v19, 0xffff0000, v19
	v_and_b32_e32 v18, 0xffff0000, v18
	v_mov_b32_e32 v22, v21
	v_lshlrev_b32_e32 v21, 16, v25
	v_lshlrev_b32_e32 v20, 16, v24
	v_and_b32_e32 v25, 0xffff0000, v25
	v_and_b32_e32 v24, 0xffff0000, v24
	v_mov_b32_e32 v42, v28
	v_mov_b32_e32 v43, v30
	v_mov_b32_e32 v30, v29
	v_lshlrev_b32_e32 v29, 16, v27
	v_lshlrev_b32_e32 v28, 16, v26
	v_and_b32_e32 v27, 0xffff0000, v27
	v_and_b32_e32 v26, 0xffff0000, v26
	v_pk_fma_f32 v[34:35], v[40:41], v[38:39], v[34:35]
	v_pk_fma_f32 v[14:15], v[22:23], v[18:19], v[14:15]
	v_mul_f32_e32 v1, 0x3d372713, v20
	v_mul_f32_e32 v18, 0x3d372713, v24
	v_mul_f32_e32 v22, 0x3d372713, v21
	v_pk_fma_f32 v[12:13], v[30:31], v[16:17], v[12:13]
	v_mul_f32_e32 v16, 0x3d372713, v25
	v_mul_f32_e32 v30, 0x3d372713, v28
	v_mul_f32_e32 v38, 0x3d372713, v29
	v_mov_b32_e32 v4, v20
	v_mov_b32_e32 v19, v24
	v_pk_fma_f32 v[10:11], v[42:43], v[36:37], v[10:11]
	v_mov_b32_e32 v23, v21
	v_mov_b32_e32 v17, v25
	v_mov_b32_e32 v31, v28
	v_mul_f32_e32 v36, 0x3d372713, v26
	v_mov_b32_e32 v39, v29
	v_mul_f32_e32 v40, 0x3d372713, v27
	v_mul_f32_e32 v1, v1, v20
	v_mul_f32_e32 v18, v18, v24
	v_mul_f32_e32 v22, v22, v21
	v_mul_f32_e32 v16, v16, v25
	v_mul_f32_e32 v30, v30, v28
	v_mul_f32_e32 v38, v38, v29
	v_mov_b32_e32 v37, v26
	v_mov_b32_e32 v41, v27
	v_mul_f32_e32 v36, v36, v26
	v_mul_f32_e32 v40, v40, v27
	v_fmac_f32_e32 v4, v1, v4
	v_fmac_f32_e32 v19, v18, v19
	v_fmac_f32_e32 v23, v22, v23
	v_fmac_f32_e32 v17, v16, v17
	v_fmac_f32_e32 v31, v30, v31
	v_fmac_f32_e32 v39, v38, v39
	v_fmac_f32_e32 v37, v36, v37
	v_fmac_f32_e32 v41, v40, v41
	v_mul_f32_e32 v1, 0x3f4c422a, v4
	v_mul_f32_e32 v4, 0x3f4c422a, v19
; __device__ __forceinline__ unsigned pk2(float lo, float hi) { return f2bf(lo) | (f2bf(hi) << 16); }
; __device__ __forceinline__ float gelu_tanh(float x) { const float y = 0.7978845608028654f * (x + 0.044715f * x * x * x); const float e = __expf(2.0f * y); return x * (1.0f - __builtin_amdgcn_rcpf(1.0f + e)); }
; __device__ __forceinline__ void lru_combine(const Params& P, size_t wi, size_t nw) {
;     ...
;         const v4u hl = HLOC[i], pc = PCUM[i], gt = GATE[i];
;         const f32x4 h0 = *(const f32x4*)(HIN + (t >> 6) * 512 + ch0), h1 = *(const f32x4*)(HIN + (t >> 6) * 512 + ch0 + 4);
;         float y[8];
;         y[0] = (bflo(hl.x) + bflo(pc.x) * h0.x) * gelu_tanh(bflo(gt.x)); y[1] = (bfhi(hl.x) + bfhi(pc.x) * h0.y) * gelu_tanh(bfhi(gt.x));
;         y[2] = (bflo(hl.y) + bflo(pc.y) * h0.z) * gelu_tanh(bflo(gt.y)); y[3] = (bfhi(hl.y) + bfhi(pc.y) * h0.w) * gelu_tanh(bfhi(gt.y));
;         y[4] = (bflo(hl.z) + bflo(pc.z) * h1.x) * gelu_tanh(bflo(gt.z)); y[5] = (bfhi(hl.z) + bfhi(pc.z) * h1.y) * gelu_tanh(bfhi(gt.z));
;         y[6] = (bflo(hl.w) + bflo(pc.w) * h1.z) * gelu_tanh(bflo(gt.w)); y[7] = (bfhi(hl.w) + bfhi(pc.w) * h1.w) * gelu_tanh(bfhi(gt.w));
;         v4u o; o.x = pk2(y[0], y[1]); o.y = pk2(y[2], y[3]); o.z = pk2(y[4], y[5]); o.w = pk2(y[6], y[7]);
;         *(v4u*)(Y + t * 1024 + 512 + ch0) = o;
	v_mul_f32_e32 v16, 0x3f4c422a, v23
	v_mul_f32_e32 v17, 0x3f4c422a, v17
	v_mul_f32_e32 v18, 0x3f4c422a, v31
	v_mul_f32_e32 v22, 0x3f4c422a, v39
	v_mul_f32_e32 v19, 0x3f4c422a, v37
	v_mul_f32_e32 v23, 0x3f4c422a, v41
	v_add_f32_e32 v1, v1, v1
	v_add_f32_e32 v4, v4, v4
	v_add_f32_e32 v16, v16, v16
	v_add_f32_e32 v17, v17, v17
	v_add_f32_e32 v18, v18, v18
	v_add_f32_e32 v22, v22, v22
	v_add_f32_e32 v19, v19, v19
	v_add_f32_e32 v23, v23, v23
	v_mul_f32_e32 v1, 0x3fb8aa3b, v1
	v_mul_f32_e32 v4, 0x3fb8aa3b, v4
	v_mul_f32_e32 v16, 0x3fb8aa3b, v16
	v_mul_f32_e32 v17, 0x3fb8aa3b, v17
	v_mul_f32_e32 v18, 0x3fb8aa3b, v18
	v_mul_f32_e32 v22, 0x3fb8aa3b, v22
	v_mul_f32_e32 v19, 0x3fb8aa3b, v19
	v_mul_f32_e32 v23, 0x3fb8aa3b, v23
	v_exp_f32_e32 v1, v1
	v_exp_f32_e32 v4, v4
	v_exp_f32_e32 v16, v16
	v_exp_f32_e32 v17, v17
	v_exp_f32_e32 v18, v18
	v_exp_f32_e32 v22, v22
	v_exp_f32_e32 v19, v19
	v_exp_f32_e32 v23, v23
	v_add_f32_e32 v1, 1.0, v1
	v_add_f32_e32 v4, 1.0, v4
	v_add_f32_e32 v30, 1.0, v16
	v_add_f32_e32 v31, 1.0, v17
	v_add_f32_e32 v36, 1.0, v18
	v_add_f32_e32 v38, 1.0, v22
	v_add_f32_e32 v37, 1.0, v19
	v_add_f32_e32 v39, 1.0, v23
	v_rcp_f32_e32 v16, v1
	v_rcp_f32_e32 v18, v4
	v_rcp_f32_e32 v17, v30
	v_rcp_f32_e32 v19, v31
	v_rcp_f32_e32 v22, v36
	v_rcp_f32_e32 v23, v38
	v_rcp_f32_e32 v30, v37
	v_rcp_f32_e32 v31, v39
	v_pk_add_f32 v[16:17], v[16:17], 1.0 op_sel_hi:[1,0] neg_lo:[1,0] neg_hi:[1,0]
	v_pk_add_f32 v[18:19], v[18:19], 1.0 op_sel_hi:[1,0] neg_lo:[1,0] neg_hi:[1,0]
	v_pk_add_f32 v[22:23], v[22:23], 1.0 op_sel_hi:[1,0] neg_lo:[1,0] neg_hi:[1,0]
	v_pk_add_f32 v[30:31], v[30:31], 1.0 op_sel_hi:[1,0] neg_lo:[1,0] neg_hi:[1,0]
	v_pk_mul_f32 v[16:17], v[16:17], v[20:21]
	v_pk_mul_f32 v[18:19], v[18:19], v[24:25]
	v_pk_mul_f32 v[20:21], v[22:23], v[28:29]
	v_pk_mul_f32 v[22:23], v[30:31], v[26:27]
	v_pk_mul_f32 v[10:11], v[10:11], v[16:17]
	v_pk_mul_f32 v[12:13], v[12:13], v[18:19]
	v_pk_mul_f32 v[16:17], v[34:35], v[20:21]
	v_pk_mul_f32 v[14:15], v[14:15], v[22:23]
	v_cvt_pk_bf16_f32 v10, v10, v12
	v_cvt_pk_bf16_f32 v11, v11, v13
	v_cvt_pk_bf16_f32 v12, v16, v14
	v_cvt_pk_bf16_f32 v13, v17, v15
	global_store_dwordx4 v[32:33], v[10:13], off offset:1024
	s_mov_b64 exec, s[100:101]
.Llc_loop:
	s_mov_b64 s[98:99], exec
	s_andn2_b64 exec, exec, s[14:15]
	s_cbranch_execz .Llc_lastB
	v_lshl_add_u64 v[10:11], s[24:25], 0, v[6:7]
	v_add_co_u32_e32 v12, vcc, 0x1c00000, v10
	v_lshrrev_b32_e32 v4, 1, v2
	s_nop 0
	v_addc_co_u32_e32 v13, vcc, 0, v11, vcc
	v_add_co_u32_e32 v16, vcc, 0x2c00000, v10
	v_and_b32_e32 v1, 0x1f8, v8
	v_and_b32_e32 v4, 0x7f800, v4
	v_addc_co_u32_e32 v17, vcc, 0, v11, vcc
	v_lshl_add_u64 v[18:19], s[18:19], 0, v[4:5]
	v_lshlrev_b32_e32 v4, 2, v1
	v_add_co_u32_e32 v10, vcc, 0x8c00000, v10
	v_and_b32_e32 v20, 0xfffc00, v6
	v_lshl_add_u64 v[28:29], v[18:19], 0, v[4:5]
	v_addc_co_u32_e32 v11, vcc, 0, v11, vcc
	global_load_dwordx4 v[12:15], v[12:13], off
	v_lshlrev_b32_e32 v4, 1, v20
	global_load_dwordx4 v[16:19], v[16:17], off
	s_nop 0
	global_load_dwordx4 v[20:23], v[28:29], off offset:16
	global_load_dwordx4 v[24:27], v[10:11], off
	s_nop 0
	global_load_dwordx4 v[28:31], v[28:29], off
	v_lshl_add_u64 v[32:33], s[94:95], 0, v[4:5]
	v_lshlrev_b32_e32 v4, 1, v1
	v_lshl_add_u64 v[10:11], v[32:33], 0, v[4:5]
	v_add_co_u32_e32 v32, vcc, 0x400000, v10
	v_lshl_add_u64 v[2:3], v[2:3], 0, s[16:17]
	s_nop 0
	v_addc_co_u32_e32 v33, vcc, 0, v11, vcc
	v_cmp_lt_u64_e64 s[0:1], s[42:43], v[2:3]
	v_lshl_add_u64 v[6:7], v[6:7], 0, s[20:21]
	v_lshl_add_u64 v[8:9], v[8:9], 0, s[12:13]
	s_or_b64 s[14:15], s[0:1], s[14:15]
	s_mov_b64 s[100:101], exec
	s_mov_b64 exec, s[98:99]
	s_waitcnt vmcnt(6)
	v_lshlrev_b32_e32 v51, 16, v53
	v_lshlrev_b32_e32 v50, 16, v52
	v_and_b32_e32 v53, 0xffff0000, v53
	v_and_b32_e32 v52, 0xffff0000, v52
	v_lshlrev_b32_e32 v75, 16, v55
	v_lshlrev_b32_e32 v74, 16, v54
	v_and_b32_e32 v55, 0xffff0000, v55
	v_and_b32_e32 v54, 0xffff0000, v54
	v_lshlrev_b32_e32 v77, 16, v57
	v_lshlrev_b32_e32 v76, 16, v56
	v_and_b32_e32 v57, 0xffff0000, v57
	v_and_b32_e32 v56, 0xffff0000, v56
	v_lshlrev_b32_e32 v79, 16, v59
	v_lshlrev_b32_e32 v78, 16, v58
	v_mov_b32_e32 v80, v60
	v_mov_b32_e32 v81, v62
	v_and_b32_e32 v59, 0xffff0000, v59
	v_and_b32_e32 v58, 0xffff0000, v58
	v_mov_b32_e32 v62, v61
	v_lshlrev_b32_e32 v61, 16, v65
	v_lshlrev_b32_e32 v60, 16, v64
	v_and_b32_e32 v65, 0xffff0000, v65
	v_and_b32_e32 v64, 0xffff0000, v64
	v_mov_b32_e32 v82, v68
	v_mov_b32_e32 v83, v70
	v_mov_b32_e32 v70, v69
	v_lshlrev_b32_e32 v69, 16, v67
	v_lshlrev_b32_e32 v68, 16, v66
	v_and_b32_e32 v67, 0xffff0000, v67
	v_and_b32_e32 v66, 0xffff0000, v66
	v_pk_fma_f32 v[74:75], v[80:81], v[78:79], v[74:75]
	v_pk_fma_f32 v[54:55], v[62:63], v[58:59], v[54:55]
	v_mul_f32_e32 v88, 0x3d372713, v60
	v_mul_f32_e32 v58, 0x3d372713, v64
	v_mul_f32_e32 v62, 0x3d372713, v61
	v_pk_fma_f32 v[52:53], v[70:71], v[56:57], v[52:53]
	v_mul_f32_e32 v56, 0x3d372713, v65
	v_mul_f32_e32 v70, 0x3d372713, v68
	v_mul_f32_e32 v78, 0x3d372713, v69
	v_mov_b32_e32 v86, v60
	v_mov_b32_e32 v59, v64
	v_pk_fma_f32 v[50:51], v[82:83], v[76:77], v[50:51]
	v_mov_b32_e32 v63, v61
	v_mov_b32_e32 v57, v65
	v_mov_b32_e32 v71, v68
	v_mul_f32_e32 v76, 0x3d372713, v66
	v_mov_b32_e32 v79, v69
	v_mul_f32_e32 v80, 0x3d372713, v67
	v_mul_f32_e32 v88, v88, v60
	v_mul_f32_e32 v58, v58, v64
	v_mul_f32_e32 v62, v62, v61
	v_mul_f32_e32 v56, v56, v65
	v_mul_f32_e32 v70, v70, v68
	v_mul_f32_e32 v78, v78, v69
	v_mov_b32_e32 v77, v66
	v_mov_b32_e32 v81, v67
	v_mul_f32_e32 v76, v76, v66
	v_mul_f32_e32 v80, v80, v67
	v_fmac_f32_e32 v86, v88, v86
	v_fmac_f32_e32 v59, v58, v59
	v_fmac_f32_e32 v63, v62, v63
	v_fmac_f32_e32 v57, v56, v57
; __device__ __forceinline__ unsigned pk2(float lo, float hi) { return f2bf(lo) | (f2bf(hi) << 16); }
; __device__ __forceinline__ float gelu_tanh(float x) { const float y = 0.7978845608028654f * (x + 0.044715f * x * x * x); const float e = __expf(2.0f * y); return x * (1.0f - __builtin_amdgcn_rcpf(1.0f + e)); }
; __device__ __forceinline__ void lru_combine(const Params& P, size_t wi, size_t nw) {
;     ...
;         const v4u hl = HLOC[i], pc = PCUM[i], gt = GATE[i];
;         const f32x4 h0 = *(const f32x4*)(HIN + (t >> 6) * 512 + ch0), h1 = *(const f32x4*)(HIN + (t >> 6) * 512 + ch0 + 4);
;         float y[8];
;         y[0] = (bflo(hl.x) + bflo(pc.x) * h0.x) * gelu_tanh(bflo(gt.x)); y[1] = (bfhi(hl.x) + bfhi(pc.x) * h0.y) * gelu_tanh(bfhi(gt.x));
;         y[2] = (bflo(hl.y) + bflo(pc.y) * h0.z) * gelu_tanh(bflo(gt.y)); y[3] = (bfhi(hl.y) + bfhi(pc.y) * h0.w) * gelu_tanh(bfhi(gt.y));
;         y[4] = (bflo(hl.z) + bflo(pc.z) * h1.x) * gelu_tanh(bflo(gt.z)); y[5] = (bfhi(hl.z) + bfhi(pc.z) * h1.y) * gelu_tanh(bfhi(gt.z));
;         y[6] = (bflo(hl.w) + bflo(pc.w) * h1.z) * gelu_tanh(bflo(gt.w)); y[7] = (bfhi(hl.w) + bfhi(pc.w) * h1.w) * gelu_tanh(bfhi(gt.w));
;         v4u o; o.x = pk2(y[0], y[1]); o.y = pk2(y[2], y[3]); o.z = pk2(y[4], y[5]); o.w = pk2(y[6], y[7]);
;         *(v4u*)(Y + t * 1024 + 512 + ch0) = o;
	v_fmac_f32_e32 v71, v70, v71
	v_fmac_f32_e32 v79, v78, v79
	v_fmac_f32_e32 v77, v76, v77
	v_fmac_f32_e32 v81, v80, v81
	v_mul_f32_e32 v88, 0x3f4c422a, v86
	v_mul_f32_e32 v86, 0x3f4c422a, v59
	v_mul_f32_e32 v56, 0x3f4c422a, v63
	v_mul_f32_e32 v57, 0x3f4c422a, v57
	v_mul_f32_e32 v58, 0x3f4c422a, v71
	v_mul_f32_e32 v62, 0x3f4c422a, v79
	v_mul_f32_e32 v59, 0x3f4c422a, v77
	v_mul_f32_e32 v63, 0x3f4c422a, v81
	v_add_f32_e32 v88, v88, v88
	v_add_f32_e32 v86, v86, v86
	v_add_f32_e32 v56, v56, v56
	v_add_f32_e32 v57, v57, v57
	v_add_f32_e32 v58, v58, v58
	v_add_f32_e32 v62, v62, v62
	v_add_f32_e32 v59, v59, v59
	v_add_f32_e32 v63, v63, v63
	v_mul_f32_e32 v88, 0x3fb8aa3b, v88
	v_mul_f32_e32 v86, 0x3fb8aa3b, v86
	v_mul_f32_e32 v56, 0x3fb8aa3b, v56
	v_mul_f32_e32 v57, 0x3fb8aa3b, v57
	v_mul_f32_e32 v58, 0x3fb8aa3b, v58
	v_mul_f32_e32 v62, 0x3fb8aa3b, v62
	v_mul_f32_e32 v59, 0x3fb8aa3b, v59
	v_mul_f32_e32 v63, 0x3fb8aa3b, v63
	v_exp_f32_e32 v88, v88
	v_exp_f32_e32 v86, v86
	v_exp_f32_e32 v56, v56
	v_exp_f32_e32 v57, v57
	v_exp_f32_e32 v58, v58
	v_exp_f32_e32 v62, v62
	v_exp_f32_e32 v59, v59
	v_exp_f32_e32 v63, v63
	v_add_f32_e32 v88, 1.0, v88
	v_add_f32_e32 v86, 1.0, v86
	v_add_f32_e32 v70, 1.0, v56
	v_add_f32_e32 v71, 1.0, v57
	v_add_f32_e32 v76, 1.0, v58
	v_add_f32_e32 v78, 1.0, v62
	v_add_f32_e32 v77, 1.0, v59
	v_add_f32_e32 v79, 1.0, v63
	v_rcp_f32_e32 v56, v88
	v_rcp_f32_e32 v58, v86
	v_rcp_f32_e32 v57, v70
	v_rcp_f32_e32 v59, v71
	v_rcp_f32_e32 v62, v76
	v_rcp_f32_e32 v63, v78
	v_rcp_f32_e32 v70, v77
	v_rcp_f32_e32 v71, v79
	v_pk_add_f32 v[56:57], v[56:57], 1.0 op_sel_hi:[1,0] neg_lo:[1,0] neg_hi:[1,0]
	v_pk_add_f32 v[58:59], v[58:59], 1.0 op_sel_hi:[1,0] neg_lo:[1,0] neg_hi:[1,0]
	v_pk_add_f32 v[62:63], v[62:63], 1.0 op_sel_hi:[1,0] neg_lo:[1,0] neg_hi:[1,0]
	v_pk_add_f32 v[70:71], v[70:71], 1.0 op_sel_hi:[1,0] neg_lo:[1,0] neg_hi:[1,0]
	v_pk_mul_f32 v[56:57], v[56:57], v[60:61]
	v_pk_mul_f32 v[58:59], v[58:59], v[64:65]
	v_pk_mul_f32 v[60:61], v[62:63], v[68:69]
	v_pk_mul_f32 v[62:63], v[70:71], v[66:67]
	v_pk_mul_f32 v[50:51], v[50:51], v[56:57]
	v_pk_mul_f32 v[52:53], v[52:53], v[58:59]
	v_pk_mul_f32 v[56:57], v[74:75], v[60:61]
	v_pk_mul_f32 v[54:55], v[54:55], v[62:63]
	v_cvt_pk_bf16_f32 v50, v50, v52
	v_cvt_pk_bf16_f32 v51, v51, v53
	v_cvt_pk_bf16_f32 v52, v56, v54
	v_cvt_pk_bf16_f32 v53, v57, v55
	global_store_dwordx4 v[72:73], v[50:53], off offset:1024
	s_mov_b64 exec, s[100:101]
	s_mov_b64 s[98:99], exec
	s_andn2_b64 exec, exec, s[14:15]
	s_cbranch_execz .Llc_lastA
	v_lshl_add_u64 v[50:51], s[24:25], 0, v[6:7]
	v_add_co_u32_e32 v52, vcc, 0x1c00000, v50
	v_lshrrev_b32_e32 v86, 1, v2
	s_nop 0
	v_addc_co_u32_e32 v53, vcc, 0, v51, vcc
	v_add_co_u32_e32 v56, vcc, 0x2c00000, v50
	v_and_b32_e32 v88, 0x1f8, v8
	v_and_b32_e32 v86, 0x7f800, v86
	v_addc_co_u32_e32 v57, vcc, 0, v51, vcc
	v_lshl_add_u64 v[58:59], s[18:19], 0, v[86:87]
	v_lshlrev_b32_e32 v86, 2, v88
	v_add_co_u32_e32 v50, vcc, 0x8c00000, v50
	v_and_b32_e32 v60, 0xfffc00, v6
	v_lshl_add_u64 v[68:69], v[58:59], 0, v[86:87]
	v_addc_co_u32_e32 v51, vcc, 0, v51, vcc
	global_load_dwordx4 v[52:55], v[52:53], off
	v_lshlrev_b32_e32 v86, 1, v60
	global_load_dwordx4 v[56:59], v[56:57], off
	s_nop 0
	global_load_dwordx4 v[60:63], v[68:69], off offset:16
	global_load_dwordx4 v[64:67], v[50:51], off
	s_nop 0
	global_load_dwordx4 v[68:71], v[68:69], off
	v_lshl_add_u64 v[72:73], s[94:95], 0, v[86:87]
	v_lshlrev_b32_e32 v86, 1, v88
	v_lshl_add_u64 v[50:51], v[72:73], 0, v[86:87]
	v_add_co_u32_e32 v72, vcc, 0x400000, v50
	v_lshl_add_u64 v[2:3], v[2:3], 0, s[16:17]
	s_nop 0
	v_addc_co_u32_e32 v73, vcc, 0, v51, vcc
	v_cmp_lt_u64_e64 s[0:1], s[42:43], v[2:3]
	v_lshl_add_u64 v[6:7], v[6:7], 0, s[20:21]
	v_lshl_add_u64 v[8:9], v[8:9], 0, s[12:13]
	s_or_b64 s[14:15], s[0:1], s[14:15]
	s_mov_b64 s[100:101], exec
	s_mov_b64 exec, s[98:99]
	s_waitcnt vmcnt(6)
	v_lshlrev_b32_e32 v11, 16, v13
	v_lshlrev_b32_e32 v10, 16, v12
	v_and_b32_e32 v13, 0xffff0000, v13
	v_and_b32_e32 v12, 0xffff0000, v12
	v_lshlrev_b32_e32 v35, 16, v15
	v_lshlrev_b32_e32 v34, 16, v14
	v_and_b32_e32 v15, 0xffff0000, v15
	v_and_b32_e32 v14, 0xffff0000, v14
	v_lshlrev_b32_e32 v37, 16, v17
	v_lshlrev_b32_e32 v36, 16, v16
	v_and_b32_e32 v17, 0xffff0000, v17
	v_and_b32_e32 v16, 0xffff0000, v16
	v_lshlrev_b32_e32 v39, 16, v19
	v_lshlrev_b32_e32 v38, 16, v18
	v_mov_b32_e32 v40, v20
	v_mov_b32_e32 v41, v22
	v_and_b32_e32 v19, 0xffff0000, v19
	v_and_b32_e32 v18, 0xffff0000, v18
	v_mov_b32_e32 v22, v21
	v_lshlrev_b32_e32 v21, 16, v25
	v_lshlrev_b32_e32 v20, 16, v24
	v_and_b32_e32 v25, 0xffff0000, v25
	v_and_b32_e32 v24, 0xffff0000, v24
	v_mov_b32_e32 v42, v28
	v_mov_b32_e32 v43, v30
	v_mov_b32_e32 v30, v29
	v_lshlrev_b32_e32 v29, 16, v27
	v_lshlrev_b32_e32 v28, 16, v26
	v_and_b32_e32 v27, 0xffff0000, v27
	v_and_b32_e32 v26, 0xffff0000, v26
	v_pk_fma_f32 v[34:35], v[40:41], v[38:39], v[34:35]
	v_pk_fma_f32 v[14:15], v[22:23], v[18:19], v[14:15]
	v_mul_f32_e32 v1, 0x3d372713, v20
	v_mul_f32_e32 v18, 0x3d372713, v24
	v_mul_f32_e32 v22, 0x3d372713, v21
	v_pk_fma_f32 v[12:13], v[30:31], v[16:17], v[12:13]
	v_mul_f32_e32 v16, 0x3d372713, v25
	v_mul_f32_e32 v30, 0x3d372713, v28
	v_mul_f32_e32 v38, 0x3d372713, v29
	v_mov_b32_e32 v4, v20
	v_mov_b32_e32 v19, v24
	v_pk_fma_f32 v[10:11], v[42:43], v[36:37], v[10:11]
	v_mov_b32_e32 v23, v21
	v_mov_b32_e32 v17, v25
	v_mov_b32_e32 v31, v28
	v_mul_f32_e32 v36, 0x3d372713, v26
	v_mov_b32_e32 v39, v29
	v_mul_f32_e32 v40, 0x3d372713, v27
	v_mul_f32_e32 v1, v1, v20
	v_mul_f32_e32 v18, v18, v24
	v_mul_f32_e32 v22, v22, v21
	v_mul_f32_e32 v16, v16, v25
	v_mul_f32_e32 v30, v30, v28
	v_mul_f32_e32 v38, v38, v29
; __device__ __forceinline__ unsigned pk2(float lo, float hi) { return f2bf(lo) | (f2bf(hi) << 16); }
; __device__ __forceinline__ float gelu_tanh(float x) { const float y = 0.7978845608028654f * (x + 0.044715f * x * x * x); const float e = __expf(2.0f * y); return x * (1.0f - __builtin_amdgcn_rcpf(1.0f + e)); }
; __device__ __forceinline__ void lru_combine(const Params& P, size_t wi, size_t nw) {
;     ...
;         const v4u hl = HLOC[i], pc = PCUM[i], gt = GATE[i];
;         const f32x4 h0 = *(const f32x4*)(HIN + (t >> 6) * 512 + ch0), h1 = *(const f32x4*)(HIN + (t >> 6) * 512 + ch0 + 4);
;         float y[8];
;         y[0] = (bflo(hl.x) + bflo(pc.x) * h0.x) * gelu_tanh(bflo(gt.x)); y[1] = (bfhi(hl.x) + bfhi(pc.x) * h0.y) * gelu_tanh(bfhi(gt.x));
;         y[2] = (bflo(hl.y) + bflo(pc.y) * h0.z) * gelu_tanh(bflo(gt.y)); y[3] = (bfhi(hl.y) + bfhi(pc.y) * h0.w) * gelu_tanh(bfhi(gt.y));
;         y[4] = (bflo(hl.z) + bflo(pc.z) * h1.x) * gelu_tanh(bflo(gt.z)); y[5] = (bfhi(hl.z) + bfhi(pc.z) * h1.y) * gelu_tanh(bfhi(gt.z));
;         y[6] = (bflo(hl.w) + bflo(pc.w) * h1.z) * gelu_tanh(bflo(gt.w)); y[7] = (bfhi(hl.w) + bfhi(pc.w) * h1.w) * gelu_tanh(bfhi(gt.w));
;         v4u o; o.x = pk2(y[0], y[1]); o.y = pk2(y[2], y[3]); o.z = pk2(y[4], y[5]); o.w = pk2(y[6], y[7]);
;         *(v4u*)(Y + t * 1024 + 512 + ch0) = o;
	v_mov_b32_e32 v37, v26
	v_mov_b32_e32 v41, v27
	v_mul_f32_e32 v36, v36, v26
	v_mul_f32_e32 v40, v40, v27
	v_fmac_f32_e32 v4, v1, v4
	v_fmac_f32_e32 v19, v18, v19
	v_fmac_f32_e32 v23, v22, v23
	v_fmac_f32_e32 v17, v16, v17
	v_fmac_f32_e32 v31, v30, v31
	v_fmac_f32_e32 v39, v38, v39
	v_fmac_f32_e32 v37, v36, v37
	v_fmac_f32_e32 v41, v40, v41
	v_mul_f32_e32 v1, 0x3f4c422a, v4
	v_mul_f32_e32 v4, 0x3f4c422a, v19
	v_mul_f32_e32 v16, 0x3f4c422a, v23
	v_mul_f32_e32 v17, 0x3f4c422a, v17
	v_mul_f32_e32 v18, 0x3f4c422a, v31
	v_mul_f32_e32 v22, 0x3f4c422a, v39
	v_mul_f32_e32 v19, 0x3f4c422a, v37
	v_mul_f32_e32 v23, 0x3f4c422a, v41
	v_add_f32_e32 v1, v1, v1
	v_add_f32_e32 v4, v4, v4
	v_add_f32_e32 v16, v16, v16
	v_add_f32_e32 v17, v17, v17
	v_add_f32_e32 v18, v18, v18
	v_add_f32_e32 v22, v22, v22
	v_add_f32_e32 v19, v19, v19
	v_add_f32_e32 v23, v23, v23
	v_mul_f32_e32 v1, 0x3fb8aa3b, v1
	v_mul_f32_e32 v4, 0x3fb8aa3b, v4
	v_mul_f32_e32 v16, 0x3fb8aa3b, v16
	v_mul_f32_e32 v17, 0x3fb8aa3b, v17
	v_mul_f32_e32 v18, 0x3fb8aa3b, v18
	v_mul_f32_e32 v22, 0x3fb8aa3b, v22
	v_mul_f32_e32 v19, 0x3fb8aa3b, v19
	v_mul_f32_e32 v23, 0x3fb8aa3b, v23
	v_exp_f32_e32 v1, v1
	v_exp_f32_e32 v4, v4
	v_exp_f32_e32 v16, v16
	v_exp_f32_e32 v17, v17
	v_exp_f32_e32 v18, v18
	v_exp_f32_e32 v22, v22
	v_exp_f32_e32 v19, v19
	v_exp_f32_e32 v23, v23
	v_add_f32_e32 v1, 1.0, v1
	v_add_f32_e32 v4, 1.0, v4
	v_add_f32_e32 v30, 1.0, v16
	v_add_f32_e32 v31, 1.0, v17
	v_add_f32_e32 v36, 1.0, v18
	v_add_f32_e32 v38, 1.0, v22
	v_add_f32_e32 v37, 1.0, v19
	v_add_f32_e32 v39, 1.0, v23
	v_rcp_f32_e32 v16, v1
	v_rcp_f32_e32 v18, v4
	v_rcp_f32_e32 v17, v30
	v_rcp_f32_e32 v19, v31
	v_rcp_f32_e32 v22, v36
	v_rcp_f32_e32 v23, v38
	v_rcp_f32_e32 v30, v37
	v_rcp_f32_e32 v31, v39
	v_pk_add_f32 v[16:17], v[16:17], 1.0 op_sel_hi:[1,0] neg_lo:[1,0] neg_hi:[1,0]
	v_pk_add_f32 v[18:19], v[18:19], 1.0 op_sel_hi:[1,0] neg_lo:[1,0] neg_hi:[1,0]
	v_pk_add_f32 v[22:23], v[22:23], 1.0 op_sel_hi:[1,0] neg_lo:[1,0] neg_hi:[1,0]
	v_pk_add_f32 v[30:31], v[30:31], 1.0 op_sel_hi:[1,0] neg_lo:[1,0] neg_hi:[1,0]
	v_pk_mul_f32 v[16:17], v[16:17], v[20:21]
	v_pk_mul_f32 v[18:19], v[18:19], v[24:25]
	v_pk_mul_f32 v[20:21], v[22:23], v[28:29]
	v_pk_mul_f32 v[22:23], v[30:31], v[26:27]
	v_pk_mul_f32 v[10:11], v[10:11], v[16:17]
	v_pk_mul_f32 v[12:13], v[12:13], v[18:19]
	v_pk_mul_f32 v[16:17], v[34:35], v[20:21]
	v_pk_mul_f32 v[14:15], v[14:15], v[22:23]
	v_cvt_pk_bf16_f32 v10, v10, v12
	v_cvt_pk_bf16_f32 v11, v11, v13
	v_cvt_pk_bf16_f32 v12, v16, v14
	v_cvt_pk_bf16_f32 v13, v17, v15
	global_store_dwordx4 v[32:33], v[10:13], off offset:1024
	s_mov_b64 exec, s[100:101]
	s_branch .Llc_loop
.Llc_lastA:
	s_mov_b64 exec, s[98:99]
	s_waitcnt vmcnt(0)
	v_lshlrev_b32_e32 v11, 16, v13
	v_lshlrev_b32_e32 v10, 16, v12
	v_and_b32_e32 v13, 0xffff0000, v13
	v_and_b32_e32 v12, 0xffff0000, v12
	v_lshlrev_b32_e32 v35, 16, v15
	v_lshlrev_b32_e32 v34, 16, v14
	v_and_b32_e32 v15, 0xffff0000, v15
	v_and_b32_e32 v14, 0xffff0000, v14
	v_lshlrev_b32_e32 v37, 16, v17
	v_lshlrev_b32_e32 v36, 16, v16
	v_and_b32_e32 v17, 0xffff0000, v17
	v_and_b32_e32 v16, 0xffff0000, v16
	v_lshlrev_b32_e32 v39, 16, v19
	v_lshlrev_b32_e32 v38, 16, v18
	v_mov_b32_e32 v40, v20
	v_mov_b32_e32 v41, v22
	v_and_b32_e32 v19, 0xffff0000, v19
	v_and_b32_e32 v18, 0xffff0000, v18
	v_mov_b32_e32 v22, v21
	v_lshlrev_b32_e32 v21, 16, v25
	v_lshlrev_b32_e32 v20, 16, v24
	v_and_b32_e32 v25, 0xffff0000, v25
	v_and_b32_e32 v24, 0xffff0000, v24
	v_mov_b32_e32 v42, v28
	v_mov_b32_e32 v43, v30
	v_mov_b32_e32 v30, v29
	v_lshlrev_b32_e32 v29, 16, v27
	v_lshlrev_b32_e32 v28, 16, v26
	v_and_b32_e32 v27, 0xffff0000, v27
	v_and_b32_e32 v26, 0xffff0000, v26
	v_pk_fma_f32 v[34:35], v[40:41], v[38:39], v[34:35]
	v_pk_fma_f32 v[14:15], v[22:23], v[18:19], v[14:15]
	v_mul_f32_e32 v1, 0x3d372713, v20
	v_mul_f32_e32 v18, 0x3d372713, v24
	v_mul_f32_e32 v22, 0x3d372713, v21
	v_pk_fma_f32 v[12:13], v[30:31], v[16:17], v[12:13]
	v_mul_f32_e32 v16, 0x3d372713, v25
	v_mul_f32_e32 v30, 0x3d372713, v28
	v_mul_f32_e32 v38, 0x3d372713, v29
	v_mov_b32_e32 v4, v20
	v_mov_b32_e32 v19, v24
	v_pk_fma_f32 v[10:11], v[42:43], v[36:37], v[10:11]
	v_mov_b32_e32 v23, v21
	v_mov_b32_e32 v17, v25
	v_mov_b32_e32 v31, v28
	v_mul_f32_e32 v36, 0x3d372713, v26
	v_mov_b32_e32 v39, v29
	v_mul_f32_e32 v40, 0x3d372713, v27
	v_mul_f32_e32 v1, v1, v20
	v_mul_f32_e32 v18, v18, v24
	v_mul_f32_e32 v22, v22, v21
	v_mul_f32_e32 v16, v16, v25
	v_mul_f32_e32 v30, v30, v28
	v_mul_f32_e32 v38, v38, v29
	v_mov_b32_e32 v37, v26
	v_mov_b32_e32 v41, v27
	v_mul_f32_e32 v36, v36, v26
	v_mul_f32_e32 v40, v40, v27
	v_fmac_f32_e32 v4, v1, v4
	v_fmac_f32_e32 v19, v18, v19
	v_fmac_f32_e32 v23, v22, v23
	v_fmac_f32_e32 v17, v16, v17
	v_fmac_f32_e32 v31, v30, v31
	v_fmac_f32_e32 v39, v38, v39
	v_fmac_f32_e32 v37, v36, v37
	v_fmac_f32_e32 v41, v40, v41
	v_mul_f32_e32 v1, 0x3f4c422a, v4
	v_mul_f32_e32 v4, 0x3f4c422a, v19
	v_mul_f32_e32 v16, 0x3f4c422a, v23
	v_mul_f32_e32 v17, 0x3f4c422a, v17
	v_mul_f32_e32 v18, 0x3f4c422a, v31
	v_mul_f32_e32 v22, 0x3f4c422a, v39
	v_mul_f32_e32 v19, 0x3f4c422a, v37
	v_mul_f32_e32 v23, 0x3f4c422a, v41
	v_add_f32_e32 v1, v1, v1
	v_add_f32_e32 v4, v4, v4
	v_add_f32_e32 v16, v16, v16
	v_add_f32_e32 v17, v17, v17
	v_add_f32_e32 v18, v18, v18
	v_add_f32_e32 v22, v22, v22
	v_add_f32_e32 v19, v19, v19
	v_add_f32_e32 v23, v23, v23
	v_mul_f32_e32 v1, 0x3fb8aa3b, v1
	v_mul_f32_e32 v4, 0x3fb8aa3b, v4
	v_mul_f32_e32 v16, 0x3fb8aa3b, v16
	v_mul_f32_e32 v17, 0x3fb8aa3b, v17
	v_mul_f32_e32 v18, 0x3fb8aa3b, v18
	v_mul_f32_e32 v22, 0x3fb8aa3b, v22
	v_mul_f32_e32 v19, 0x3fb8aa3b, v19
	v_mul_f32_e32 v23, 0x3fb8aa3b, v23
	v_exp_f32_e32 v1, v1
; __device__ __forceinline__ unsigned pk2(float lo, float hi) { return f2bf(lo) | (f2bf(hi) << 16); }
; __device__ __forceinline__ float gelu_tanh(float x) { const float y = 0.7978845608028654f * (x + 0.044715f * x * x * x); const float e = __expf(2.0f * y); return x * (1.0f - __builtin_amdgcn_rcpf(1.0f + e)); }
; __device__ __forceinline__ void lru_combine(const Params& P, size_t wi, size_t nw) {
;     ...
;         const v4u hl = HLOC[i], pc = PCUM[i], gt = GATE[i];
;         const f32x4 h0 = *(const f32x4*)(HIN + (t >> 6) * 512 + ch0), h1 = *(const f32x4*)(HIN + (t >> 6) * 512 + ch0 + 4);
;         float y[8];
;         y[0] = (bflo(hl.x) + bflo(pc.x) * h0.x) * gelu_tanh(bflo(gt.x)); y[1] = (bfhi(hl.x) + bfhi(pc.x) * h0.y) * gelu_tanh(bfhi(gt.x));
;         y[2] = (bflo(hl.y) + bflo(pc.y) * h0.z) * gelu_tanh(bflo(gt.y)); y[3] = (bfhi(hl.y) + bfhi(pc.y) * h0.w) * gelu_tanh(bfhi(gt.y));
;         y[4] = (bflo(hl.z) + bflo(pc.z) * h1.x) * gelu_tanh(bflo(gt.z)); y[5] = (bfhi(hl.z) + bfhi(pc.z) * h1.y) * gelu_tanh(bfhi(gt.z));
;         y[6] = (bflo(hl.w) + bflo(pc.w) * h1.z) * gelu_tanh(bflo(gt.w)); y[7] = (bfhi(hl.w) + bfhi(pc.w) * h1.w) * gelu_tanh(bfhi(gt.w));
;         v4u o; o.x = pk2(y[0], y[1]); o.y = pk2(y[2], y[3]); o.z = pk2(y[4], y[5]); o.w = pk2(y[6], y[7]);
;         *(v4u*)(Y + t * 1024 + 512 + ch0) = o;
	v_exp_f32_e32 v4, v4
	v_exp_f32_e32 v16, v16
	v_exp_f32_e32 v17, v17
	v_exp_f32_e32 v18, v18
	v_exp_f32_e32 v22, v22
	v_exp_f32_e32 v19, v19
	v_exp_f32_e32 v23, v23
	v_add_f32_e32 v1, 1.0, v1
	v_add_f32_e32 v4, 1.0, v4
	v_add_f32_e32 v30, 1.0, v16
	v_add_f32_e32 v31, 1.0, v17
	v_add_f32_e32 v36, 1.0, v18
	v_add_f32_e32 v38, 1.0, v22
	v_add_f32_e32 v37, 1.0, v19
	v_add_f32_e32 v39, 1.0, v23
	v_rcp_f32_e32 v16, v1
	v_rcp_f32_e32 v18, v4
	v_rcp_f32_e32 v17, v30
	v_rcp_f32_e32 v19, v31
	v_rcp_f32_e32 v22, v36
	v_rcp_f32_e32 v23, v38
	v_rcp_f32_e32 v30, v37
	v_rcp_f32_e32 v31, v39
	v_pk_add_f32 v[16:17], v[16:17], 1.0 op_sel_hi:[1,0] neg_lo:[1,0] neg_hi:[1,0]
	v_pk_add_f32 v[18:19], v[18:19], 1.0 op_sel_hi:[1,0] neg_lo:[1,0] neg_hi:[1,0]
	v_pk_add_f32 v[22:23], v[22:23], 1.0 op_sel_hi:[1,0] neg_lo:[1,0] neg_hi:[1,0]
	v_pk_add_f32 v[30:31], v[30:31], 1.0 op_sel_hi:[1,0] neg_lo:[1,0] neg_hi:[1,0]
	v_pk_mul_f32 v[16:17], v[16:17], v[20:21]
	v_pk_mul_f32 v[18:19], v[18:19], v[24:25]
	v_pk_mul_f32 v[20:21], v[22:23], v[28:29]
	v_pk_mul_f32 v[22:23], v[30:31], v[26:27]
	v_pk_mul_f32 v[10:11], v[10:11], v[16:17]
	v_pk_mul_f32 v[12:13], v[12:13], v[18:19]
	v_pk_mul_f32 v[16:17], v[34:35], v[20:21]
	v_pk_mul_f32 v[14:15], v[14:15], v[22:23]
	v_cvt_pk_bf16_f32 v10, v10, v12
	v_cvt_pk_bf16_f32 v11, v11, v13
	v_cvt_pk_bf16_f32 v12, v16, v14
	v_cvt_pk_bf16_f32 v13, v17, v15
	global_store_dwordx4 v[32:33], v[10:13], off offset:1024
	s_branch .Llc_done
.Llc_lastB:
	s_mov_b64 exec, s[98:99]
	s_waitcnt vmcnt(0)
	v_lshlrev_b32_e32 v51, 16, v53
	v_lshlrev_b32_e32 v50, 16, v52
	v_and_b32_e32 v53, 0xffff0000, v53
	v_and_b32_e32 v52, 0xffff0000, v52
	v_lshlrev_b32_e32 v75, 16, v55
	v_lshlrev_b32_e32 v74, 16, v54
	v_and_b32_e32 v55, 0xffff0000, v55
	v_and_b32_e32 v54, 0xffff0000, v54
	v_lshlrev_b32_e32 v77, 16, v57
	v_lshlrev_b32_e32 v76, 16, v56
	v_and_b32_e32 v57, 0xffff0000, v57
	v_and_b32_e32 v56, 0xffff0000, v56
	v_lshlrev_b32_e32 v79, 16, v59
	v_lshlrev_b32_e32 v78, 16, v58
	v_mov_b32_e32 v80, v60
	v_mov_b32_e32 v81, v62
	v_and_b32_e32 v59, 0xffff0000, v59
	v_and_b32_e32 v58, 0xffff0000, v58
	v_mov_b32_e32 v62, v61
	v_lshlrev_b32_e32 v61, 16, v65
	v_lshlrev_b32_e32 v60, 16, v64
	v_and_b32_e32 v65, 0xffff0000, v65
	v_and_b32_e32 v64, 0xffff0000, v64
	v_mov_b32_e32 v82, v68
	v_mov_b32_e32 v83, v70
	v_mov_b32_e32 v70, v69
	v_lshlrev_b32_e32 v69, 16, v67
	v_lshlrev_b32_e32 v68, 16, v66
	v_and_b32_e32 v67, 0xffff0000, v67
	v_and_b32_e32 v66, 0xffff0000, v66
	v_pk_fma_f32 v[74:75], v[80:81], v[78:79], v[74:75]
	v_pk_fma_f32 v[54:55], v[62:63], v[58:59], v[54:55]
	v_mul_f32_e32 v88, 0x3d372713, v60
	v_mul_f32_e32 v58, 0x3d372713, v64
	v_mul_f32_e32 v62, 0x3d372713, v61
	v_pk_fma_f32 v[52:53], v[70:71], v[56:57], v[52:53]
	v_mul_f32_e32 v56, 0x3d372713, v65
	v_mul_f32_e32 v70, 0x3d372713, v68
	v_mul_f32_e32 v78, 0x3d372713, v69
	v_mov_b32_e32 v86, v60
	v_mov_b32_e32 v59, v64
	v_pk_fma_f32 v[50:51], v[82:83], v[76:77], v[50:51]
	v_mov_b32_e32 v63, v61
	v_mov_b32_e32 v57, v65
	v_mov_b32_e32 v71, v68
	v_mul_f32_e32 v76, 0x3d372713, v66
	v_mov_b32_e32 v79, v69
	v_mul_f32_e32 v80, 0x3d372713, v67
	v_mul_f32_e32 v88, v88, v60
	v_mul_f32_e32 v58, v58, v64
	v_mul_f32_e32 v62, v62, v61
	v_mul_f32_e32 v56, v56, v65
	v_mul_f32_e32 v70, v70, v68
	v_mul_f32_e32 v78, v78, v69
	v_mov_b32_e32 v77, v66
	v_mov_b32_e32 v81, v67
	v_mul_f32_e32 v76, v76, v66
	v_mul_f32_e32 v80, v80, v67
	v_fmac_f32_e32 v86, v88, v86
	v_fmac_f32_e32 v59, v58, v59
	v_fmac_f32_e32 v63, v62, v63
	v_fmac_f32_e32 v57, v56, v57
	v_fmac_f32_e32 v71, v70, v71
	v_fmac_f32_e32 v79, v78, v79
	v_fmac_f32_e32 v77, v76, v77
	v_fmac_f32_e32 v81, v80, v81
	v_mul_f32_e32 v88, 0x3f4c422a, v86
	v_mul_f32_e32 v86, 0x3f4c422a, v59
	v_mul_f32_e32 v56, 0x3f4c422a, v63
	v_mul_f32_e32 v57, 0x3f4c422a, v57
	v_mul_f32_e32 v58, 0x3f4c422a, v71
	v_mul_f32_e32 v62, 0x3f4c422a, v79
	v_mul_f32_e32 v59, 0x3f4c422a, v77
	v_mul_f32_e32 v63, 0x3f4c422a, v81
	v_add_f32_e32 v88, v88, v88
	v_add_f32_e32 v86, v86, v86
	v_add_f32_e32 v56, v56, v56
	v_add_f32_e32 v57, v57, v57
	v_add_f32_e32 v58, v58, v58
	v_add_f32_e32 v62, v62, v62
	v_add_f32_e32 v59, v59, v59
	v_add_f32_e32 v63, v63, v63
	v_mul_f32_e32 v88, 0x3fb8aa3b, v88
	v_mul_f32_e32 v86, 0x3fb8aa3b, v86
	v_mul_f32_e32 v56, 0x3fb8aa3b, v56
	v_mul_f32_e32 v57, 0x3fb8aa3b, v57
	v_mul_f32_e32 v58, 0x3fb8aa3b, v58
	v_mul_f32_e32 v62, 0x3fb8aa3b, v62
	v_mul_f32_e32 v59, 0x3fb8aa3b, v59
	v_mul_f32_e32 v63, 0x3fb8aa3b, v63
	v_exp_f32_e32 v88, v88
	v_exp_f32_e32 v86, v86
	v_exp_f32_e32 v56, v56
	v_exp_f32_e32 v57, v57
	v_exp_f32_e32 v58, v58
	v_exp_f32_e32 v62, v62
	v_exp_f32_e32 v59, v59
	v_exp_f32_e32 v63, v63
	v_add_f32_e32 v88, 1.0, v88
	v_add_f32_e32 v86, 1.0, v86
	v_add_f32_e32 v70, 1.0, v56
	v_add_f32_e32 v71, 1.0, v57
	v_add_f32_e32 v76, 1.0, v58
	v_add_f32_e32 v78, 1.0, v62
	v_add_f32_e32 v77, 1.0, v59
	v_add_f32_e32 v79, 1.0, v63
	v_rcp_f32_e32 v56, v88
	v_rcp_f32_e32 v58, v86
	v_rcp_f32_e32 v57, v70
	v_rcp_f32_e32 v59, v71
	v_rcp_f32_e32 v62, v76
	v_rcp_f32_e32 v63, v78
	v_rcp_f32_e32 v70, v77
	v_rcp_f32_e32 v71, v79
	v_pk_add_f32 v[56:57], v[56:57], 1.0 op_sel_hi:[1,0] neg_lo:[1,0] neg_hi:[1,0]
	v_pk_add_f32 v[58:59], v[58:59], 1.0 op_sel_hi:[1,0] neg_lo:[1,0] neg_hi:[1,0]
	v_pk_add_f32 v[62:63], v[62:63], 1.0 op_sel_hi:[1,0] neg_lo:[1,0] neg_hi:[1,0]
	v_pk_add_f32 v[70:71], v[70:71], 1.0 op_sel_hi:[1,0] neg_lo:[1,0] neg_hi:[1,0]
	v_pk_mul_f32 v[56:57], v[56:57], v[60:61]
	v_pk_mul_f32 v[58:59], v[58:59], v[64:65]
	v_pk_mul_f32 v[60:61], v[62:63], v[68:69]
	v_pk_mul_f32 v[62:63], v[70:71], v[66:67]
	v_pk_mul_f32 v[50:51], v[50:51], v[56:57]
	v_pk_mul_f32 v[52:53], v[52:53], v[58:59]
	v_pk_mul_f32 v[56:57], v[74:75], v[60:61]
	v_pk_mul_f32 v[54:55], v[54:55], v[62:63]
	v_cvt_pk_bf16_f32 v50, v50, v52
	v_cvt_pk_bf16_f32 v51, v51, v53
	v_cvt_pk_bf16_f32 v52, v56, v54
	v_cvt_pk_bf16_f32 v53, v57, v55
	global_store_dwordx4 v[72:73], v[50:53], off offset:1024
.Llc_done:
.LBB0_2049:
	s_or_b64 exec, exec, s[6:7]
	s_mov_b64 s[0:1], 0
